# baseline (speedup 1.0000x reference)
.LBB3_64:
	s_add_i32 s4, 0, 0x1f000
	v_add_u32_e32 v111, s4, v108
	s_mov_b64 s[6:7], 0x100
	v_readfirstlane_b32 s4, v111
	v_add_u32_e32 v3, 0x2000, v111
	v_lshl_add_u64 v[4:5], v[100:101], 0, s[6:7]
	s_mov_b32 m0, s4
	v_readfirstlane_b32 s4, v3
	v_add_u32_e32 v3, 0x4000, v111
	v_readfirstlane_b32 s70, v0
	s_nop 3
	s_lshr_b32 s70, s70, 6
	s_lshl_b32 s70, s70, 10
	s_add_i32 s76, s70, 0x5000
	s_add_i32 s77, s70, 0x7000
	s_add_i32 s78, s70, 0x9000
	s_add_i32 s79, s70, 0xb000
	s_add_i32 s80, s70, 0x0
	s_add_i32 s81, s70, 0x2000
	s_add_i32 s82, s70, 0x12000
	s_add_i32 s83, s70, 0x14000
	s_add_i32 s84, s70, 0x16000
	s_add_i32 s85, s70, 0x18000
	s_add_i32 s86, s70, 0xd000
	s_add_i32 s87, s70, 0xf000
	s_add_i32 s88, s70, 0x1f000
	s_add_i32 s89, s70, 0x21000
	s_add_i32 s90, s70, 0x23000
	s_add_i32 s91, s70, 0x25000
	s_add_i32 s92, s70, 0x1a000
	s_add_i32 s93, s70, 0x1c000
	v_subrev_u32_e32 v168, s66, v100
	v_subrev_u32_e32 v169, s66, v98
	v_subrev_u32_e32 v170, s66, v96
	v_subrev_u32_e32 v171, s66, v94
	v_subrev_u32_e32 v172, s68, v104
	v_subrev_u32_e32 v173, s68, v102
	v_subrev_u32_e32 v174, s68, v106
	s_barrier
	v_lshl_add_u64 v[4:5], v[98:99], 0, s[6:7]
	s_mov_b32 m0, s4
	v_readfirstlane_b32 s4, v3
	v_add_u32_e32 v3, 0x6000, v111
	s_add_i32 s17, 0, 0x1a000
	v_lshl_add_u64 v[4:5], v[96:97], 0, s[6:7]
	s_mov_b32 m0, s4
	v_readfirstlane_b32 s4, v3
	v_add_u32_e32 v112, s17, v108
	v_lshl_add_u64 v[4:5], v[94:95], 0, s[6:7]
	s_mov_b32 m0, s4
	v_readfirstlane_b32 s4, v112
	v_add_u32_e32 v3, 0x2000, v112
	v_lshl_add_u64 v[4:5], v[104:105], 0, s[6:7]
	s_mov_b32 m0, s4
	v_readfirstlane_b32 s4, v3
	v_lshl_add_u64 v[4:5], v[102:103], 0, s[6:7]
	s_mov_b32 m0, s4
	s_and_b64 vcc, exec, s[2:3]
	s_mov_b32 s4, 0
	s_cbranch_vccnz .LBB3_66
	s_add_i32 s5, 0, 0x1e000
	v_add_u32_e32 v3, s5, v108
	v_lshl_add_u64 v[4:5], v[106:107], 0, s[6:7]
	v_readfirstlane_b32 s5, v3
	s_mov_b32 m0, s5
	s_nop 0
	global_load_lds_dwordx4 v[4:5], off

.LBB3_83:
	v_add_u32_e32 v82, s18, v115
	v_add_u32_e32 v118, 0x5000, v82
	v_or_b32_e32 v115, v118, v116
	v_add_u32_e32 v124, 0, v115
	ds_read_b128 v[86:89], v124 offset:53248
	ds_read_b128 v[90:93], v124 offset:55296
	ds_read_b128 v[82:85], v136 offset:53248
	ds_read_b128 v[138:141], v136 offset:55296
	s_and_b64 vcc, exec, s[4:5]
	s_waitcnt lgkmcnt(0)
	v_mfma_f32_16x16x32_f16 v[18:21], v[86:89], v[82:85], v[18:21]
	s_mov_b32 m0, s76
	v_mfma_f32_16x16x32_f16 v[22:25], v[90:93], v[82:85], v[22:25]
	global_load_lds_dwordx4 v168, s[72:73]
	v_mfma_f32_16x16x32_f16 v[26:29], v[86:89], v[138:141], v[26:29]
	s_mov_b32 m0, s77
	v_mfma_f32_16x16x32_f16 v[30:33], v[90:93], v[138:141], v[30:33]
	global_load_lds_dwordx4 v169, s[72:73]
	ds_read_b128 v[82:85], v136 offset:57344
	ds_read_b128 v[138:141], v136 offset:59392
	s_waitcnt lgkmcnt(0)
	v_mfma_f32_16x16x32_f16 v[34:37], v[86:89], v[82:85], v[34:37]
	s_mov_b32 m0, s78
	v_mfma_f32_16x16x32_f16 v[38:41], v[90:93], v[82:85], v[38:41]
	global_load_lds_dwordx4 v170, s[72:73]
	v_mfma_f32_16x16x32_f16 v[42:45], v[86:89], v[138:141], v[42:45]
	s_mov_b32 m0, s79
	v_mfma_f32_16x16x32_f16 v[46:49], v[90:93], v[138:141], v[46:49]
	global_load_lds_dwordx4 v171, s[72:73]
	ds_read_b128 v[82:85], v136 offset:61440
	ds_read_b128 v[140:143], v136 offset:63488
	v_add_u32_e32 v138, 0xd000, v136
	s_waitcnt lgkmcnt(0)
	ds_read_b128 v[176:179], v138 offset:16384
	v_mfma_f32_16x16x32_f16 v[50:53], v[86:89], v[82:85], v[50:53]
	s_mov_b32 m0, s80
	v_mfma_f32_16x16x32_f16 v[54:57], v[90:93], v[82:85], v[54:57]
	global_load_lds_dwordx4 v172, s[74:75]
	v_mfma_f32_16x16x32_f16 v[62:65], v[86:89], v[140:143], v[62:65]
	s_mov_b32 m0, s81
	v_mfma_f32_16x16x32_f16 v[82:85], v[90:93], v[140:143], v[58:61]
	global_load_lds_dwordx4 v173, s[74:75]
	s_cmp_lg_u64 s[2:3], 0
	s_cbranch_scc1 .Ld3_1_0
	s_add_i32 m0, s70, 0x4000
	s_nop 0
	global_load_lds_dwordx4 v174, s[74:75]
.Ld3_1_0:
	s_nop 2
	ds_read_b128 v[58:61], v138 offset:12288
	ds_read_b128 v[140:143], v138 offset:14336
	s_waitcnt lgkmcnt(0)
	v_mfma_f32_16x16x32_f16 v[66:69], v[86:89], v[58:61], v[66:69]
	v_mfma_f32_16x16x32_f16 v[70:73], v[90:93], v[58:61], v[70:73]
	v_mfma_f32_16x16x32_f16 v[74:77], v[86:89], v[140:143], v[74:77]
	v_mfma_f32_16x16x32_f16 v[78:81], v[90:93], v[140:143], v[78:81]
	s_cbranch_vccnz .LBB3_85
	s_waitcnt lgkmcnt(0)
	v_mfma_f32_16x16x32_f16 v[10:13], v[86:89], v[176:179], v[10:13]
	v_mfma_f32_16x16x32_f16 v[14:17], v[90:93], v[176:179], v[14:17]

.LBB3_94:
	s_and_b64 vcc, exec, s[4:5]
	s_waitcnt lgkmcnt(5)
	v_mfma_f32_16x16x32_f16 v[22:25], v[86:89], v[118:121], v[22:25]
	s_mov_b32 m0, s82
	v_mfma_f32_16x16x32_f16 v[18:21], v[82:85], v[118:121], v[18:21]
	global_load_lds_dwordx4 v168, s[72:73]
	s_waitcnt lgkmcnt(4)
	v_mfma_f32_16x16x32_f16 v[26:29], v[82:85], v[142:145], v[26:29]
	s_mov_b32 m0, s83
	v_mfma_f32_16x16x32_f16 v[30:33], v[86:89], v[142:145], v[30:33]
	global_load_lds_dwordx4 v169, s[72:73]
	s_waitcnt lgkmcnt(3)
	v_mfma_f32_16x16x32_f16 v[34:37], v[82:85], v[148:151], v[34:37]
	s_mov_b32 m0, s84
	v_mfma_f32_16x16x32_f16 v[38:41], v[86:89], v[148:151], v[38:41]
	global_load_lds_dwordx4 v170, s[72:73]
	ds_read_b128 v[148:151], v125 offset:12288
	s_waitcnt lgkmcnt(3)
	v_mfma_f32_16x16x32_f16 v[42:45], v[82:85], v[152:155], v[42:45]
	s_mov_b32 m0, s85
	v_mfma_f32_16x16x32_f16 v[46:49], v[86:89], v[152:155], v[46:49]
	global_load_lds_dwordx4 v171, s[72:73]
	ds_read_b128 v[152:155], v125 offset:14336
	s_waitcnt lgkmcnt(3)
	ds_read_b128 v[176:179], v125 offset:16384
	v_mfma_f32_16x16x32_f16 v[50:53], v[82:85], v[156:159], v[50:53]
	s_mov_b32 m0, s86
	v_mfma_f32_16x16x32_f16 v[54:57], v[86:89], v[156:159], v[54:57]
	global_load_lds_dwordx4 v172, s[74:75]
	s_waitcnt lgkmcnt(3)
	v_mfma_f32_16x16x32_f16 v[58:61], v[82:85], v[160:163], v[58:61]
	s_mov_b32 m0, s87
	v_mfma_f32_16x16x32_f16 v[62:65], v[86:89], v[160:163], v[62:65]
	global_load_lds_dwordx4 v173, s[74:75]
	s_cmp_lg_u64 s[2:3], 0
	s_cbranch_scc1 .Ld3_1_1
	s_add_i32 m0, s70, 0x11000
	s_nop 0
	global_load_lds_dwordx4 v174, s[74:75]
.Ld3_1_1:
	s_waitcnt lgkmcnt(2)
	v_mfma_f32_16x16x32_f16 v[66:69], v[82:85], v[148:151], v[66:69]
	v_mfma_f32_16x16x32_f16 v[70:73], v[86:89], v[148:151], v[70:73]
	s_waitcnt lgkmcnt(1)
	v_mfma_f32_16x16x32_f16 v[74:77], v[82:85], v[152:155], v[74:77]
	v_mfma_f32_16x16x32_f16 v[78:81], v[86:89], v[152:155], v[78:81]
	s_cbranch_vccnz .LBB3_96
	s_waitcnt lgkmcnt(0)
	v_mfma_f32_16x16x32_f16 v[10:13], v[82:85], v[176:179], v[10:13]
	v_mfma_f32_16x16x32_f16 v[14:17], v[86:89], v[176:179], v[14:17]

.LBB3_108:
	s_waitcnt lgkmcnt(0)
	ds_read_b128 v[82:85], v122 offset:20480
	ds_read_b128 v[86:89], v122 offset:22528
	ds_read_b128 v[112:115], v136
	ds_read_b128 v[116:119], v136 offset:2048
	ds_read_b128 v[148:151], v136 offset:4096
	ds_read_b128 v[152:155], v136 offset:6144
	ds_read_b128 v[156:159], v136 offset:8192
	ds_read_b128 v[160:163], v136 offset:10240
	s_and_b64 vcc, exec, s[4:5]
	s_waitcnt lgkmcnt(5)
	v_mfma_f32_16x16x32_f16 v[18:21], v[82:85], v[112:115], v[18:21]
	s_mov_b32 m0, s88
	v_mfma_f32_16x16x32_f16 v[22:25], v[86:89], v[112:115], v[22:25]
	global_load_lds_dwordx4 v168, s[72:73]
	s_waitcnt lgkmcnt(4)
	v_mfma_f32_16x16x32_f16 v[26:29], v[82:85], v[116:119], v[26:29]
	s_mov_b32 m0, s89
	v_mfma_f32_16x16x32_f16 v[30:33], v[86:89], v[116:119], v[30:33]
	global_load_lds_dwordx4 v169, s[72:73]
	s_waitcnt lgkmcnt(3)
	v_mfma_f32_16x16x32_f16 v[34:37], v[82:85], v[148:151], v[34:37]
	s_mov_b32 m0, s90
	v_mfma_f32_16x16x32_f16 v[38:41], v[86:89], v[148:151], v[38:41]
	global_load_lds_dwordx4 v170, s[72:73]
	ds_read_b128 v[148:151], v136 offset:12288
	s_waitcnt lgkmcnt(3)
	v_mfma_f32_16x16x32_f16 v[42:45], v[82:85], v[152:155], v[42:45]
	s_mov_b32 m0, s91
	v_mfma_f32_16x16x32_f16 v[46:49], v[86:89], v[152:155], v[46:49]
	global_load_lds_dwordx4 v171, s[72:73]
	ds_read_b128 v[152:155], v136 offset:14336
	s_waitcnt lgkmcnt(3)
	ds_read_b128 v[176:179], v136 offset:16384
	v_mfma_f32_16x16x32_f16 v[50:53], v[82:85], v[156:159], v[50:53]
	s_mov_b32 m0, s92
	v_mfma_f32_16x16x32_f16 v[54:57], v[86:89], v[156:159], v[54:57]
	global_load_lds_dwordx4 v172, s[74:75]
	s_waitcnt lgkmcnt(3)
	v_mfma_f32_16x16x32_f16 v[58:61], v[82:85], v[160:163], v[58:61]
	s_mov_b32 m0, s93
	v_mfma_f32_16x16x32_f16 v[62:65], v[86:89], v[160:163], v[62:65]
	global_load_lds_dwordx4 v173, s[74:75]
	s_cmp_lg_u64 s[2:3], 0
	s_cbranch_scc1 .Ld3_1_2
	s_add_i32 m0, s70, 0x1e000
	s_nop 0
	global_load_lds_dwordx4 v174, s[74:75]

.LBB3_119:
	s_and_b64 vcc, exec, s[4:5]
	s_waitcnt lgkmcnt(5)
	v_mfma_f32_16x16x32_f16 v[18:21], v[82:85], v[112:115], v[18:21]
	s_mov_b32 m0, s76
	v_mfma_f32_16x16x32_f16 v[22:25], v[86:89], v[112:115], v[22:25]
	global_load_lds_dwordx4 v168, s[72:73]
	s_waitcnt lgkmcnt(4)
	v_mfma_f32_16x16x32_f16 v[26:29], v[82:85], v[116:119], v[26:29]
	s_mov_b32 m0, s77
	v_mfma_f32_16x16x32_f16 v[30:33], v[86:89], v[116:119], v[30:33]
	global_load_lds_dwordx4 v169, s[72:73]
	s_waitcnt lgkmcnt(3)
	v_mfma_f32_16x16x32_f16 v[34:37], v[82:85], v[148:151], v[34:37]
	s_mov_b32 m0, s78
	v_mfma_f32_16x16x32_f16 v[38:41], v[86:89], v[148:151], v[38:41]
	global_load_lds_dwordx4 v170, s[72:73]
	ds_read_b128 v[148:151], v138 offset:12288
	s_waitcnt lgkmcnt(3)
	v_mfma_f32_16x16x32_f16 v[42:45], v[82:85], v[152:155], v[42:45]
	s_mov_b32 m0, s79
	v_mfma_f32_16x16x32_f16 v[46:49], v[86:89], v[152:155], v[46:49]
	global_load_lds_dwordx4 v171, s[72:73]
	ds_read_b128 v[152:155], v138 offset:14336
	s_waitcnt lgkmcnt(3)
	ds_read_b128 v[176:179], v138 offset:16384
	v_mfma_f32_16x16x32_f16 v[50:53], v[82:85], v[156:159], v[50:53]
	s_mov_b32 m0, s80
	v_mfma_f32_16x16x32_f16 v[54:57], v[86:89], v[156:159], v[54:57]
	global_load_lds_dwordx4 v172, s[74:75]
	s_waitcnt lgkmcnt(3)
	v_mfma_f32_16x16x32_f16 v[58:61], v[82:85], v[160:163], v[58:61]
	s_mov_b32 m0, s81
	v_mfma_f32_16x16x32_f16 v[62:65], v[86:89], v[160:163], v[62:65]
	global_load_lds_dwordx4 v173, s[74:75]
	s_cmp_lg_u64 s[2:3], 0
	s_cbranch_scc1 .Ld3_1_3
	s_add_i32 m0, s70, 0x4000
	s_nop 0
	global_load_lds_dwordx4 v174, s[74:75]

.LBB3_130:
	s_and_b64 vcc, exec, s[4:5]
	s_waitcnt lgkmcnt(5)
	v_mfma_f32_16x16x32_f16 v[18:21], v[114:117], v[82:85], v[18:21]
	s_mov_b32 m0, s82
	v_mfma_f32_16x16x32_f16 v[22:25], v[118:121], v[82:85], v[22:25]
	global_load_lds_dwordx4 v168, s[72:73]
	s_waitcnt lgkmcnt(4)
	v_mfma_f32_16x16x32_f16 v[26:29], v[114:117], v[86:89], v[26:29]
	s_mov_b32 m0, s83
	v_mfma_f32_16x16x32_f16 v[30:33], v[118:121], v[86:89], v[30:33]
	global_load_lds_dwordx4 v169, s[72:73]
	s_waitcnt lgkmcnt(2)
	v_mfma_f32_16x16x32_f16 v[42:45], v[114:117], v[152:155], v[42:45]
	s_mov_b32 m0, s84
	v_mfma_f32_16x16x32_f16 v[46:49], v[118:121], v[152:155], v[46:49]
	global_load_lds_dwordx4 v170, s[72:73]
	v_mfma_f32_16x16x32_f16 v[34:37], v[114:117], v[148:151], v[34:37]
	s_mov_b32 m0, s85
	v_mfma_f32_16x16x32_f16 v[38:41], v[118:121], v[148:151], v[38:41]
	global_load_lds_dwordx4 v171, s[72:73]
	ds_read_b128 v[148:151], v125 offset:12288
	ds_read_b128 v[152:155], v125 offset:14336
	s_waitcnt lgkmcnt(3)
	ds_read_b128 v[176:179], v125 offset:16384
	v_mfma_f32_16x16x32_f16 v[82:85], v[114:117], v[156:159], v[50:53]
	s_mov_b32 m0, s86
	v_mfma_f32_16x16x32_f16 v[86:89], v[118:121], v[156:159], v[54:57]
	global_load_lds_dwordx4 v172, s[74:75]
	s_nop 1
	s_waitcnt lgkmcnt(3)
	v_mfma_f32_16x16x32_f16 v[90:93], v[114:117], v[160:163], v[58:61]
	s_mov_b32 m0, s87
	v_mfma_f32_16x16x32_f16 v[94:97], v[118:121], v[160:163], v[62:65]
	global_load_lds_dwordx4 v173, s[74:75]
	s_cmp_lg_u64 s[2:3], 0
	s_cbranch_scc1 .Ld3_1_4
	s_add_i32 m0, s70, 0x11000
	s_nop 0
	global_load_lds_dwordx4 v174, s[74:75]
.Ld3_1_4:
	s_waitcnt lgkmcnt(2)
	v_mfma_f32_16x16x32_f16 v[98:101], v[114:117], v[148:151], v[66:69]
	v_mfma_f32_16x16x32_f16 v[102:105], v[118:121], v[148:151], v[70:73]
	s_waitcnt lgkmcnt(1)
	v_mfma_f32_16x16x32_f16 v[106:109], v[114:117], v[152:155], v[74:77]
	v_mfma_f32_16x16x32_f16 v[110:113], v[118:121], v[152:155], v[78:81]
	s_cbranch_vccnz .LBB3_132
	s_waitcnt lgkmcnt(0)
	v_mfma_f32_16x16x32_f16 v[10:13], v[114:117], v[176:179], v[10:13]
	v_mfma_f32_16x16x32_f16 v[14:17], v[118:121], v[176:179], v[14:17]

.LBB4_85:
	s_add_i32 s27, 0, 0x1f000
	v_add_u32_e32 v144, s27, v1
	s_mov_b64 s[24:25], 0x100
	v_readfirstlane_b32 s27, v144
	v_add_u32_e32 v23, 0x2000, v144
	v_lshl_add_u64 v[34:35], v[116:117], 0, s[24:25]
	s_mov_b32 m0, s27
	v_readfirstlane_b32 s27, v23
	v_add_u32_e32 v23, 0x4000, v144
	v_readfirstlane_b32 s70, v0
	s_nop 3
	s_lshr_b32 s70, s70, 6
	s_lshl_b32 s70, s70, 10
	s_add_i32 s76, s70, 0x5000
	s_add_i32 s77, s70, 0x7000
	s_add_i32 s78, s70, 0x9000
	s_add_i32 s79, s70, 0xb000
	s_add_i32 s80, s70, 0x0
	s_add_i32 s81, s70, 0x2000
	s_add_i32 s82, s70, 0x12000
	s_add_i32 s83, s70, 0x14000
	s_add_i32 s84, s70, 0x16000
	s_add_i32 s85, s70, 0x18000
	s_add_i32 s86, s70, 0xd000
	s_add_i32 s87, s70, 0xf000
	s_add_i32 s88, s70, 0x1f000
	s_add_i32 s89, s70, 0x21000
	s_add_i32 s90, s70, 0x23000
	s_add_i32 s91, s70, 0x25000
	s_add_i32 s92, s70, 0x1a000
	s_add_i32 s93, s70, 0x1c000
	v_subrev_u32_e32 v176, s66, v116
	v_subrev_u32_e32 v177, s66, v114
	v_subrev_u32_e32 v178, s66, v112
	v_subrev_u32_e32 v179, s66, v110
	v_subrev_u32_e32 v180, s68, v120
	v_subrev_u32_e32 v181, s68, v118
	s_add_u32 s72, s66, 0x100
	s_addc_u32 s73, s67, 0
	s_add_u32 s74, s68, 0x100
	s_addc_u32 s75, s69, 0
	v_subrev_u32_e32 v182, s68, v122
	s_barrier
	s_add_i32 s35, 0, 0x1a000
	v_add_u32_e32 v145, s35, v1
	v_readfirstlane_b32 s27, v145
	s_and_b64 vcc, exec, s[14:15]
	s_cbranch_vccnz .LBB4_87
	v_lshl_add_u64 v[34:35], v[122:123], 0, s[24:25]
	s_add_i32 s24, 0, 0x1e000
	v_add_u32_e32 v23, s24, v1
	s_nop 0
	v_readfirstlane_b32 s24, v23
	s_mov_b32 m0, s24
	s_nop 0
	global_load_lds_dwordx4 v[34:35], off

.LBB4_98:
	v_add_u32_e32 v82, s36, v140
	v_add_u32_e32 v107, 0x5000, v82
	v_or_b32_e32 v106, v107, v141
	v_add_u32_e32 v142, 0, v106
	ds_read_b128 v[98:101], v142 offset:53248
	ds_read_b128 v[102:105], v142 offset:55296
	ds_read_b128 v[82:85], v137 offset:53248
	ds_read_b128 v[86:89], v137 offset:55296
	v_add_u32_e32 v140, 0xd000, v137
	s_and_b64 vcc, exec, s[24:25]
	s_waitcnt lgkmcnt(0)
	v_mfma_f32_16x16x32_f16 v[34:37], v[98:101], v[82:85], v[34:37]
	s_mov_b32 m0, s76
	v_mfma_f32_16x16x32_f16 v[38:41], v[102:105], v[82:85], v[38:41]
	global_load_lds_dwordx4 v176, s[72:73]
	v_mfma_f32_16x16x32_f16 v[42:45], v[98:101], v[86:89], v[42:45]
	s_mov_b32 m0, s77
	v_mfma_f32_16x16x32_f16 v[46:49], v[102:105], v[86:89], v[46:49]
	global_load_lds_dwordx4 v177, s[72:73]
	ds_read_b128 v[82:85], v137 offset:57344
	ds_read_b128 v[86:89], v137 offset:59392
	s_waitcnt lgkmcnt(0)
	v_mfma_f32_16x16x32_f16 v[50:53], v[98:101], v[82:85], v[50:53]
	s_mov_b32 m0, s78
	v_mfma_f32_16x16x32_f16 v[54:57], v[102:105], v[82:85], v[54:57]
	global_load_lds_dwordx4 v178, s[72:73]
	v_mfma_f32_16x16x32_f16 v[58:61], v[98:101], v[86:89], v[58:61]
	s_mov_b32 m0, s79
	v_mfma_f32_16x16x32_f16 v[62:65], v[102:105], v[86:89], v[62:65]
	global_load_lds_dwordx4 v179, s[72:73]
	ds_read_b128 v[82:85], v137 offset:61440
	ds_read_b128 v[86:89], v137 offset:63488
	s_waitcnt lgkmcnt(0)
	ds_read_b128 v[184:187], v140 offset:16384
	v_mfma_f32_16x16x32_f16 v[66:69], v[98:101], v[82:85], v[66:69]
	s_mov_b32 m0, s80
	v_mfma_f32_16x16x32_f16 v[70:73], v[102:105], v[82:85], v[70:73]
	global_load_lds_dwordx4 v180, s[74:75]
	v_mfma_f32_16x16x32_f16 v[82:85], v[102:105], v[86:89], v[18:21]
	s_nop 2
	ds_read_b128 v[18:21], v140 offset:12288
	ds_read_b128 v[148:151], v140 offset:14336
	s_mov_b32 m0, s81
	v_mfma_f32_16x16x32_f16 v[74:77], v[98:101], v[86:89], v[74:77]
	global_load_lds_dwordx4 v181, s[74:75]
	s_cmp_lg_u64 s[14:15], 0
	s_cbranch_scc1 .Ld3_2_0
	s_add_i32 m0, s70, 0x4000
	s_nop 0
	global_load_lds_dwordx4 v182, s[74:75]
.Ld3_2_0:
	s_waitcnt lgkmcnt(0)
	v_mfma_f32_16x16x32_f16 v[86:89], v[98:101], v[18:21], v[22:25]
	v_mfma_f32_16x16x32_f16 v[90:93], v[102:105], v[18:21], v[26:29]
	v_mfma_f32_16x16x32_f16 v[94:97], v[98:101], v[148:151], v[30:33]
	v_mfma_f32_16x16x32_f16 v[78:81], v[102:105], v[148:151], v[78:81]
	s_cbranch_vccnz .LBB4_100
	s_waitcnt lgkmcnt(0)
	v_mfma_f32_16x16x32_f16 v[6:9], v[98:101], v[184:187], v[6:9]
	v_mfma_f32_16x16x32_f16 v[2:5], v[102:105], v[184:187], v[2:5]

.LBB4_109:
	s_and_b64 vcc, exec, s[24:25]
	s_waitcnt lgkmcnt(5)
	v_mfma_f32_16x16x32_f16 v[22:25], v[86:89], v[92:95], v[22:25]
	s_mov_b32 m0, s82
	v_mfma_f32_16x16x32_f16 v[18:21], v[82:85], v[92:95], v[18:21]
	global_load_lds_dwordx4 v176, s[72:73]
	s_waitcnt lgkmcnt(4)
	v_mfma_f32_16x16x32_f16 v[26:29], v[82:85], v[96:99], v[26:29]
	s_mov_b32 m0, s83
	v_mfma_f32_16x16x32_f16 v[30:33], v[86:89], v[96:99], v[30:33]
	global_load_lds_dwordx4 v177, s[72:73]
	s_waitcnt lgkmcnt(3)
	v_mfma_f32_16x16x32_f16 v[34:37], v[82:85], v[156:159], v[34:37]
	s_mov_b32 m0, s84
	v_mfma_f32_16x16x32_f16 v[38:41], v[86:89], v[156:159], v[38:41]
	global_load_lds_dwordx4 v178, s[72:73]
	ds_read_b128 v[156:159], v146 offset:12288
	s_waitcnt lgkmcnt(3)
	v_mfma_f32_16x16x32_f16 v[42:45], v[82:85], v[160:163], v[42:45]
	s_mov_b32 m0, s85
	v_mfma_f32_16x16x32_f16 v[46:49], v[86:89], v[160:163], v[46:49]
	global_load_lds_dwordx4 v179, s[72:73]
	ds_read_b128 v[160:163], v146 offset:14336
	s_waitcnt lgkmcnt(3)
	ds_read_b128 v[184:187], v146 offset:16384
	v_mfma_f32_16x16x32_f16 v[50:53], v[82:85], v[164:167], v[50:53]
	s_mov_b32 m0, s86
	v_mfma_f32_16x16x32_f16 v[54:57], v[86:89], v[164:167], v[54:57]
	global_load_lds_dwordx4 v180, s[74:75]
	s_waitcnt lgkmcnt(3)
	v_mfma_f32_16x16x32_f16 v[58:61], v[82:85], v[168:171], v[58:61]
	s_mov_b32 m0, s87
	v_mfma_f32_16x16x32_f16 v[62:65], v[86:89], v[168:171], v[62:65]
	global_load_lds_dwordx4 v181, s[74:75]
	s_cmp_lg_u64 s[14:15], 0
	s_cbranch_scc1 .Ld3_2_1
	s_add_i32 m0, s70, 0x11000
	s_nop 0
	global_load_lds_dwordx4 v182, s[74:75]
.Ld3_2_1:
	s_waitcnt lgkmcnt(2)
	v_mfma_f32_16x16x32_f16 v[66:69], v[82:85], v[156:159], v[66:69]
	v_mfma_f32_16x16x32_f16 v[70:73], v[86:89], v[156:159], v[70:73]
	s_waitcnt lgkmcnt(1)
	v_mfma_f32_16x16x32_f16 v[74:77], v[82:85], v[160:163], v[74:77]
	v_mfma_f32_16x16x32_f16 v[78:81], v[86:89], v[160:163], v[78:81]
	s_cbranch_vccnz .LBB4_111
	s_waitcnt lgkmcnt(0)
	v_mfma_f32_16x16x32_f16 v[6:9], v[82:85], v[184:187], v[6:9]
	v_mfma_f32_16x16x32_f16 v[2:5], v[86:89], v[184:187], v[2:5]

.LBB4_123:
	s_and_b64 vcc, exec, s[24:25]
	s_waitcnt lgkmcnt(5)
	v_mfma_f32_16x16x32_f16 v[18:21], v[82:85], v[92:95], v[18:21]
	s_mov_b32 m0, s88
	v_mfma_f32_16x16x32_f16 v[22:25], v[86:89], v[92:95], v[22:25]
	global_load_lds_dwordx4 v176, s[72:73]
	s_waitcnt lgkmcnt(4)
	v_mfma_f32_16x16x32_f16 v[26:29], v[82:85], v[96:99], v[26:29]
	s_mov_b32 m0, s89
	v_mfma_f32_16x16x32_f16 v[30:33], v[86:89], v[96:99], v[30:33]
	global_load_lds_dwordx4 v177, s[72:73]
	s_waitcnt lgkmcnt(3)
	v_mfma_f32_16x16x32_f16 v[34:37], v[82:85], v[156:159], v[34:37]
	s_mov_b32 m0, s90
	v_mfma_f32_16x16x32_f16 v[38:41], v[86:89], v[156:159], v[38:41]
	global_load_lds_dwordx4 v178, s[72:73]
	ds_read_b128 v[156:159], v137 offset:12288
	s_waitcnt lgkmcnt(3)
	v_mfma_f32_16x16x32_f16 v[42:45], v[82:85], v[160:163], v[42:45]
	s_mov_b32 m0, s91
	v_mfma_f32_16x16x32_f16 v[46:49], v[86:89], v[160:163], v[46:49]
	global_load_lds_dwordx4 v179, s[72:73]
	ds_read_b128 v[160:163], v137 offset:14336
	s_waitcnt lgkmcnt(3)
	ds_read_b128 v[184:187], v137 offset:16384
	v_mfma_f32_16x16x32_f16 v[50:53], v[82:85], v[164:167], v[50:53]
	s_mov_b32 m0, s92
	v_mfma_f32_16x16x32_f16 v[54:57], v[86:89], v[164:167], v[54:57]
	global_load_lds_dwordx4 v180, s[74:75]
	s_waitcnt lgkmcnt(3)
	v_mfma_f32_16x16x32_f16 v[58:61], v[82:85], v[168:171], v[58:61]
	s_mov_b32 m0, s93
	v_mfma_f32_16x16x32_f16 v[62:65], v[86:89], v[168:171], v[62:65]
	global_load_lds_dwordx4 v181, s[74:75]
	s_cmp_lg_u64 s[14:15], 0
	s_cbranch_scc1 .Ld3_2_2
	s_add_i32 m0, s70, 0x1e000
	s_nop 0
	global_load_lds_dwordx4 v182, s[74:75]

.LBB4_134:
	s_and_b64 vcc, exec, s[24:25]
	s_waitcnt lgkmcnt(5)
	v_mfma_f32_16x16x32_f16 v[18:21], v[82:85], v[92:95], v[18:21]
	s_mov_b32 m0, s76
	v_mfma_f32_16x16x32_f16 v[22:25], v[86:89], v[92:95], v[22:25]
	global_load_lds_dwordx4 v176, s[72:73]
	s_waitcnt lgkmcnt(4)
	v_mfma_f32_16x16x32_f16 v[26:29], v[82:85], v[96:99], v[26:29]
	s_mov_b32 m0, s77
	v_mfma_f32_16x16x32_f16 v[30:33], v[86:89], v[96:99], v[30:33]
	global_load_lds_dwordx4 v177, s[72:73]
	s_waitcnt lgkmcnt(3)
	v_mfma_f32_16x16x32_f16 v[34:37], v[82:85], v[156:159], v[34:37]
	s_mov_b32 m0, s78
	v_mfma_f32_16x16x32_f16 v[38:41], v[86:89], v[156:159], v[38:41]
	global_load_lds_dwordx4 v178, s[72:73]
	ds_read_b128 v[156:159], v140 offset:12288
	s_waitcnt lgkmcnt(3)
	v_mfma_f32_16x16x32_f16 v[42:45], v[82:85], v[160:163], v[42:45]
	s_mov_b32 m0, s79
	v_mfma_f32_16x16x32_f16 v[46:49], v[86:89], v[160:163], v[46:49]
	global_load_lds_dwordx4 v179, s[72:73]
	ds_read_b128 v[160:163], v140 offset:14336
	s_waitcnt lgkmcnt(3)
	ds_read_b128 v[184:187], v140 offset:16384
	v_mfma_f32_16x16x32_f16 v[50:53], v[82:85], v[164:167], v[50:53]
	s_mov_b32 m0, s80
	v_mfma_f32_16x16x32_f16 v[54:57], v[86:89], v[164:167], v[54:57]
	global_load_lds_dwordx4 v180, s[74:75]
	s_waitcnt lgkmcnt(3)
	v_mfma_f32_16x16x32_f16 v[58:61], v[82:85], v[168:171], v[58:61]
	s_mov_b32 m0, s81
	v_mfma_f32_16x16x32_f16 v[62:65], v[86:89], v[168:171], v[62:65]
	global_load_lds_dwordx4 v181, s[74:75]
	s_cmp_lg_u64 s[14:15], 0
	s_cbranch_scc1 .Ld3_2_3
	s_add_i32 m0, s70, 0x4000
	s_nop 0
	global_load_lds_dwordx4 v182, s[74:75]

.LBB4_145:
	s_waitcnt lgkmcnt(0)
	ds_read_b128 v[114:117], v90
	ds_read_b128 v[118:121], v90 offset:2048
	ds_read_b128 v[82:85], v146
	ds_read_b128 v[86:89], v146 offset:2048
	ds_read_b128 v[156:159], v146 offset:4096
	ds_read_b128 v[160:163], v146 offset:6144
	ds_read_b128 v[164:167], v146 offset:8192
	ds_read_b128 v[168:171], v146 offset:10240
	s_and_b64 vcc, exec, s[24:25]
	s_waitcnt lgkmcnt(5)
	v_mfma_f32_16x16x32_f16 v[18:21], v[114:117], v[82:85], v[18:21]
	s_mov_b32 m0, s82
	v_mfma_f32_16x16x32_f16 v[22:25], v[118:121], v[82:85], v[22:25]
	global_load_lds_dwordx4 v176, s[72:73]
	s_waitcnt lgkmcnt(4)
	v_mfma_f32_16x16x32_f16 v[26:29], v[114:117], v[86:89], v[26:29]
	s_mov_b32 m0, s83
	v_mfma_f32_16x16x32_f16 v[30:33], v[118:121], v[86:89], v[30:33]
	global_load_lds_dwordx4 v177, s[72:73]
	s_waitcnt lgkmcnt(2)
	v_mfma_f32_16x16x32_f16 v[42:45], v[114:117], v[160:163], v[42:45]
	s_mov_b32 m0, s84
	v_mfma_f32_16x16x32_f16 v[46:49], v[118:121], v[160:163], v[46:49]
	global_load_lds_dwordx4 v178, s[72:73]
	v_mfma_f32_16x16x32_f16 v[34:37], v[114:117], v[156:159], v[34:37]
	s_mov_b32 m0, s85
	v_mfma_f32_16x16x32_f16 v[38:41], v[118:121], v[156:159], v[38:41]
	global_load_lds_dwordx4 v179, s[72:73]
	ds_read_b128 v[156:159], v146 offset:12288
	ds_read_b128 v[160:163], v146 offset:14336
	s_waitcnt lgkmcnt(3)
	ds_read_b128 v[184:187], v146 offset:16384
	v_mfma_f32_16x16x32_f16 v[82:85], v[114:117], v[164:167], v[50:53]
	s_mov_b32 m0, s86
	v_mfma_f32_16x16x32_f16 v[86:89], v[118:121], v[164:167], v[54:57]
	global_load_lds_dwordx4 v180, s[74:75]
	s_nop 1
	s_waitcnt lgkmcnt(3)
	v_mfma_f32_16x16x32_f16 v[90:93], v[114:117], v[168:171], v[58:61]
	s_mov_b32 m0, s87
	v_mfma_f32_16x16x32_f16 v[94:97], v[118:121], v[168:171], v[62:65]
	global_load_lds_dwordx4 v181, s[74:75]
	s_cmp_lg_u64 s[14:15], 0
	s_cbranch_scc1 .Ld3_2_4
	s_add_i32 m0, s70, 0x11000
	s_nop 0
	global_load_lds_dwordx4 v182, s[74:75]
.Ld3_2_4:
	s_waitcnt lgkmcnt(2)
	v_mfma_f32_16x16x32_f16 v[98:101], v[114:117], v[156:159], v[66:69]
	v_mfma_f32_16x16x32_f16 v[102:105], v[118:121], v[156:159], v[70:73]
	s_waitcnt lgkmcnt(1)
	v_mfma_f32_16x16x32_f16 v[106:109], v[114:117], v[160:163], v[74:77]
	v_mfma_f32_16x16x32_f16 v[110:113], v[118:121], v[160:163], v[78:81]
	s_cbranch_vccnz .LBB4_147
	s_waitcnt lgkmcnt(0)
	v_mfma_f32_16x16x32_f16 v[6:9], v[114:117], v[184:187], v[6:9]
	v_mfma_f32_16x16x32_f16 v[2:5], v[118:121], v[184:187], v[2:5]
